# speedup vs baseline: 1.0042x; 1.0024x over previous
.LBB0_36:
	s_cmp_ge_i32 s98, s82
	s_cselect_b64 s[82:83], -1, 0
	s_and_b64 vcc, exec, s[82:83]
	v_cvt_pkrtz_f16_f32 v158, v98, v99
	v_cvt_pkrtz_f16_f32 v159, v100, v101
	v_cvt_pkrtz_f16_f32 v222, v102, v103
	v_cvt_pkrtz_f16_f32 v223, v104, v105
	v_cvt_pkrtz_f16_f32 v154, v106, v107
	v_cvt_pkrtz_f16_f32 v155, v108, v109
	v_cvt_pkrtz_f16_f32 v220, v110, v111
	v_cvt_pkrtz_f16_f32 v221, v112, v113
	v_cvt_pkrtz_f16_f32 v150, v82, v83
	v_cvt_pkrtz_f16_f32 v151, v84, v85
	v_cvt_pkrtz_f16_f32 v218, v86, v87
	v_cvt_pkrtz_f16_f32 v219, v88, v89
	v_cvt_pkrtz_f16_f32 v146, v90, v91
	v_cvt_pkrtz_f16_f32 v147, v92, v93
	v_cvt_pkrtz_f16_f32 v16, v94, v95
	v_cvt_pkrtz_f16_f32 v17, v96, v97
	s_cbranch_vccnz .LBB0_42
	v_mov_b32_e32 v2, v0
	s_lshl_b32 s4, s98, 6
	v_ashrrev_i32_e32 v10, 4, v2
	v_lshlrev_b32_e32 v2, 2, v2
	v_and_or_b32 v2, v2, 60, s90
	v_lshl_add_u32 v11, s95, 6, v10
	v_lshlrev_b64 v[8:9], 2, v[2:3]
	v_min_i32_e32 v2, s96, v11
	v_lshl_add_u64 v[4:5], s[70:71], 0, v[8:9]
	v_add_lshl_u32 v2, v2, s76, 10
	v_lshl_add_u64 v[6:7], v[2:3], 2, v[4:5]
	v_add_u32_e32 v2, 32, v11
	v_min_i32_e32 v2, s96, v2
	v_add_lshl_u32 v2, v2, s76, 10
	v_add_u32_e32 v18, s4, v10
	v_lshl_add_u64 v[4:5], v[2:3], 2, v[4:5]
	v_min_i32_e32 v2, s96, v18
	v_lshl_add_u64 v[8:9], s[74:75], 0, v[8:9]
	v_add_lshl_u32 v2, v2, s76, 10
	v_lshl_add_u64 v[10:11], v[2:3], 2, v[8:9]
	v_add_u32_e32 v2, 32, v18
	v_min_i32_e32 v2, s96, v2
	v_add_lshl_u32 v2, v2, s76, 10
	v_lshl_add_u64 v[8:9], v[2:3], 2, v[8:9]
	global_load_dwordx4 v[12:15], v[6:7], off
	global_load_dwordx4 v[4:7], v[4:5], off
	global_load_dwordx4 v[114:117], v[10:11], off
	global_load_dwordx4 v[8:11], v[8:9], off
	s_andn2_b32 s5, 1, s98
	s_mulk_i32 s5, 0x2080
	v_add_u32_e32 v2, s5, v234
	s_setprio 1
	ds_read_b64_tr_b16 v[214:215], v2 offset:24576
	ds_read_b64_tr_b16 v[216:217], v2 offset:25088
	v_add_f32_e32 v18, v98, v99
	v_add_f32_e32 v18, v100, v18
	v_add_f32_e32 v18, v101, v18
	v_add_f32_e32 v18, v102, v18
	v_add_f32_e32 v34, v103, v18
	v_mfma_f32_32x32x16_f16 v[18:33], v[206:209], v[174:177], v[130:145]
	v_mov_b64_e32 v[212:213], v[160:161]
	v_mov_b64_e32 v[210:211], v[158:159]
	ds_read_b64_tr_b16 v[206:207], v2 offset:28736
	ds_read_b64_tr_b16 v[208:209], v2 offset:29248
	v_add_f32_e32 v34, v104, v34
	v_add_f32_e32 v34, v105, v34
	v_add_f32_e32 v34, v106, v34
	v_add_f32_e32 v34, v107, v34
	v_mov_b32_e32 v212, v222
	v_mov_b32_e32 v213, v223
	v_mfma_f32_32x32x16_f16 v[130:145], v[202:205], v[174:177], v[130:145]
	ds_read_b64_tr_b16 v[202:203], v2 offset:25600
	ds_read_b64_tr_b16 v[204:205], v2 offset:26112
	v_mfma_f32_32x32x16_f16 v[18:33], v[198:201], v[170:173], v[18:33]
	v_add_f32_e32 v34, v108, v34
	v_add_f32_e32 v34, v109, v34
	v_add_f32_e32 v34, v110, v34
	v_mov_b64_e32 v[176:177], v[156:157]
	v_add_f32_e32 v34, v111, v34
	v_mov_b64_e32 v[174:175], v[154:155]
	ds_read_b64_tr_b16 v[198:199], v2 offset:29760
	ds_read_b64_tr_b16 v[200:201], v2 offset:30272
	v_add_f32_e32 v34, v112, v34
	v_add_f32_e32 v34, v113, v34
	v_add_f32_e32 v34, v82, v34
	v_add_f32_e32 v34, v83, v34
	v_mov_b32_e32 v176, v220
	v_mov_b32_e32 v177, v221
	v_mfma_f32_32x32x16_f16 v[130:145], v[194:197], v[170:173], v[130:145]
	ds_read_b64_tr_b16 v[194:195], v2 offset:26624
	ds_read_b64_tr_b16 v[196:197], v2 offset:27136
	v_mfma_f32_32x32x16_f16 v[18:33], v[190:193], v[166:169], v[18:33]
	v_add_f32_e32 v34, v84, v34
	v_add_f32_e32 v34, v85, v34
	v_add_f32_e32 v34, v86, v34
	v_mov_b64_e32 v[122:123], v[150:151]
	v_add_f32_e32 v34, v87, v34
	v_mov_b64_e32 v[124:125], v[152:153]
	ds_read_b64_tr_b16 v[170:171], v2 offset:30784
	ds_read_b64_tr_b16 v[172:173], v2 offset:31296
	v_add_f32_e32 v34, v88, v34
	v_add_f32_e32 v34, v89, v34
	v_add_f32_e32 v34, v90, v34
	v_add_f32_e32 v34, v91, v34
	v_mov_b32_e32 v124, v218
	v_mov_b32_e32 v125, v219
	v_mfma_f32_32x32x16_f16 v[130:145], v[186:189], v[166:169], v[130:145]
	ds_read_b64_tr_b16 v[166:167], v2 offset:27648
	ds_read_b64_tr_b16 v[168:169], v2 offset:28160
	v_mfma_f32_32x32x16_f16 v[18:33], v[182:185], v[162:165], v[18:33]
	v_add_f32_e32 v34, v92, v34
	v_add_f32_e32 v34, v93, v34
	v_add_f32_e32 v34, v94, v34
	v_mov_b64_e32 v[118:119], v[146:147]
	v_add_f32_e32 v152, v95, v34
	v_mov_b64_e32 v[120:121], v[148:149]
	ds_read_b64_tr_b16 v[126:127], v2 offset:31808
	ds_read_b64_tr_b16 v[128:129], v2 offset:32320
	s_nop 0
	v_mov_b64_e32 v[34:35], v[130:131]
	v_mov_b64_e32 v[36:37], v[132:133]
	v_mov_b64_e32 v[38:39], v[134:135]
	v_mov_b64_e32 v[40:41], v[136:137]
	v_mov_b64_e32 v[42:43], v[138:139]
	v_mov_b64_e32 v[44:45], v[140:141]
	v_mov_b64_e32 v[46:47], v[142:143]
	v_mov_b64_e32 v[48:49], v[144:145]
	v_add_f32_e32 v2, v96, v152
	v_add_f32_e32 v2, v97, v2
	v_mfma_f32_32x32x16_f16 v[34:49], v[178:181], v[162:165], v[34:49]
	v_add_f32_e32 v2, 0, v2
	v_mov_b32_e32 v120, v16
	v_mov_b32_e32 v121, v17
	s_setprio 0
	s_cmp_lg_u32 s98, s95
	s_cselect_b64 s[6:7], -1, 0
	s_or_b64 s[6:7], s[6:7], s[80:81]
	s_and_b64 vcc, exec, s[6:7]
	s_cbranch_vccnz .LBB0_39
	v_mov_b32_e32 v130, v229
	s_nop 0
	v_ashrrev_i32_e32 v130, 3, v130
	v_and_b32_e32 v130, -4, v130
	v_add_u32_e32 v130, s4, v130
	v_add_u32_e32 v131, 32, v130
	v_cmp_gt_i32_e32 vcc, s3, v131
	v_or_b32_e32 v131, 1, v130
	v_cmp_gt_i32_e64 s[30:31], s3, v131
	v_add_u32_e32 v131, 33, v130
	v_cmp_gt_i32_e64 s[40:41], s3, v131
	v_or_b32_e32 v131, 2, v130
	v_cmp_gt_i32_e64 s[36:37], s3, v131
	v_add_u32_e32 v131, 34, v130
	v_cmp_gt_i32_e64 s[4:5], s3, v131
	v_or_b32_e32 v131, 3, v130
	v_cmp_gt_i32_e64 s[38:39], s3, v131
	v_add_u32_e32 v131, 35, v130
	v_cmp_gt_i32_e64 s[6:7], s3, v131
	v_add_u32_e32 v131, 8, v130
	v_cmp_gt_i32_e64 s[42:43], s3, v131
	v_add_u32_e32 v131, 40, v130
	v_cmp_gt_i32_e64 s[8:9], s3, v131
	v_add_u32_e32 v131, 9, v130
	v_cmp_gt_i32_e64 s[44:45], s3, v131
	v_add_u32_e32 v131, 41, v130
	v_cmp_gt_i32_e64 s[10:11], s3, v131
	v_add_u32_e32 v131, 10, v130
	v_cmp_gt_i32_e64 s[46:47], s3, v131
	v_add_u32_e32 v131, 42, v130
	v_cmp_gt_i32_e64 s[12:13], s3, v131
	v_add_u32_e32 v131, 11, v130
	v_cmp_gt_i32_e64 s[48:49], s3, v131
	v_add_u32_e32 v131, 43, v130
	v_cmp_gt_i32_e64 s[14:15], s3, v131
	v_add_u32_e32 v131, 16, v130
	v_cmp_gt_i32_e64 s[50:51], s3, v131
	v_add_u32_e32 v131, 48, v130
	v_cmp_gt_i32_e64 s[16:17], s3, v131
	v_add_u32_e32 v131, 17, v130
	v_cmp_gt_i32_e64 s[52:53], s3, v131
	v_add_u32_e32 v131, 49, v130
	v_cmp_gt_i32_e64 s[18:19], s3, v131
	v_add_u32_e32 v131, 18, v130
	v_cmp_gt_i32_e64 s[54:55], s3, v131
	v_add_u32_e32 v131, 50, v130
	v_cmp_gt_i32_e64 s[20:21], s3, v131
	v_add_u32_e32 v131, 19, v130
	v_cmp_gt_i32_e64 s[56:57], s3, v131
	v_add_u32_e32 v131, 51, v130
	v_cmp_gt_i32_e64 s[22:23], s3, v131
	v_add_u32_e32 v131, 24, v130
	v_cmp_gt_i32_e64 s[58:59], s3, v131
	v_add_u32_e32 v131, 56, v130
	v_cmp_gt_i32_e64 s[24:25], s3, v131
	v_add_u32_e32 v131, 25, v130
	v_cmp_gt_i32_e64 s[60:61], s3, v131
	v_add_u32_e32 v131, 57, v130
	v_cmp_gt_i32_e64 s[28:29], s3, v131
	v_add_u32_e32 v131, 26, v130
	v_cmp_gt_i32_e64 s[62:63], s3, v131
	v_add_u32_e32 v131, 58, v130
	v_cmp_gt_i32_e64 s[34:35], s3, v131
	v_add_u32_e32 v131, 27, v130
	v_cmp_gt_i32_e64 s[64:65], s3, v131
	s_or_b64 s[62:63], s[64:65], s[62:63]
	s_or_b64 s[60:61], s[62:63], s[60:61]
	s_or_b64 s[58:59], s[60:61], s[58:59]
	s_or_b64 s[56:57], s[58:59], s[56:57]
	s_or_b64 s[54:55], s[56:57], s[54:55]
	s_or_b64 s[52:53], s[54:55], s[52:53]
	s_or_b64 s[50:51], s[52:53], s[50:51]
	s_or_b64 s[48:49], s[50:51], s[48:49]
	s_or_b64 s[46:47], s[48:49], s[46:47]
	s_or_b64 s[44:45], s[46:47], s[44:45]
	s_or_b64 s[42:43], s[44:45], s[42:43]
	s_or_b64 s[38:39], s[42:43], s[38:39]
	s_or_b64 s[36:37], s[38:39], s[36:37]
	v_cmp_gt_i32_e64 s[26:27], s3, v130
	s_or_b64 s[30:31], s[36:37], s[30:31]
	s_or_b64 s[26:27], s[30:31], s[26:27]
	v_add_u32_e32 v130, 59, v130
	v_cndmask_b32_e64 v18, v242, v18, s[26:27]
	v_cmp_gt_i32_e64 s[26:27], s3, v130
	v_cndmask_b32_e64 v33, v242, v33, s[64:65]
	v_cndmask_b32_e64 v32, v242, v32, s[62:63]
	v_cndmask_b32_e64 v49, v242, v49, s[26:27]
	s_or_b64 s[26:27], s[26:27], s[34:35]
	v_cndmask_b32_e64 v48, v242, v48, s[26:27]
	s_or_b64 s[26:27], s[26:27], s[28:29]
	s_or_b64 s[24:25], s[26:27], s[24:25]
	s_or_b64 s[22:23], s[24:25], s[22:23]
	s_or_b64 s[20:21], s[22:23], s[20:21]
	s_or_b64 s[18:19], s[20:21], s[18:19]
	s_or_b64 s[16:17], s[18:19], s[16:17]
	s_or_b64 s[14:15], s[16:17], s[14:15]
	s_or_b64 s[12:13], s[14:15], s[12:13]
	s_or_b64 s[10:11], s[12:13], s[10:11]
	s_or_b64 s[8:9], s[10:11], s[8:9]
	s_or_b64 s[6:7], s[8:9], s[6:7]
	s_or_b64 s[4:5], s[6:7], s[4:5]
	v_cndmask_b32_e64 v36, v242, v36, s[4:5]
	s_or_b64 s[4:5], s[4:5], s[40:41]
	s_or_b64 vcc, s[4:5], vcc
	v_cndmask_b32_e64 v31, v242, v31, s[60:61]
	v_cndmask_b32_e64 v30, v242, v30, s[58:59]
	v_cndmask_b32_e64 v29, v242, v29, s[56:57]
	v_cndmask_b32_e64 v28, v242, v28, s[54:55]
	v_cndmask_b32_e64 v27, v242, v27, s[52:53]
	v_cndmask_b32_e64 v26, v242, v26, s[50:51]
	v_cndmask_b32_e64 v25, v242, v25, s[48:49]
	v_cndmask_b32_e64 v24, v242, v24, s[46:47]
	v_cndmask_b32_e64 v23, v242, v23, s[44:45]
	v_cndmask_b32_e64 v22, v242, v22, s[42:43]
	v_cndmask_b32_e64 v21, v242, v21, s[38:39]
	v_cndmask_b32_e64 v20, v242, v20, s[36:37]
	v_cndmask_b32_e64 v19, v242, v19, s[30:31]
	v_cndmask_b32_e64 v47, v242, v47, s[26:27]
	v_cndmask_b32_e64 v46, v242, v46, s[24:25]
	v_cndmask_b32_e64 v45, v242, v45, s[22:23]
	v_cndmask_b32_e64 v44, v242, v44, s[20:21]
	v_cndmask_b32_e64 v43, v242, v43, s[18:19]
	v_cndmask_b32_e64 v42, v242, v42, s[16:17]
	v_cndmask_b32_e64 v41, v242, v41, s[14:15]
	v_cndmask_b32_e64 v40, v242, v40, s[12:13]
	v_cndmask_b32_e64 v39, v242, v39, s[10:11]
	v_cndmask_b32_e64 v38, v242, v38, s[8:9]
	v_cndmask_b32_e64 v37, v242, v37, s[6:7]
	v_cndmask_b32_e64 v35, v242, v35, s[4:5]
	v_cndmask_b32_e32 v34, v242, v34, vcc
